# layer-0 in-proj epilogue: the eight per-row-group 1/rms loads issued together (one wait) instead of a load + full drain per row group; SB work-queue atomic prefetched one unit ahead
# speedup vs baseline: 1.0299x; 1.0022x over previous
; __device__ __forceinline__ unsigned f2bf(float f) { unsigned u = __builtin_bit_cast(unsigned, f); return (u + 0x7fffu + ((u >> 16) & 1u)) >> 16; }
; __device__ __forceinline__ u32x4 pack8(f32x4 a, f32x4 b) { u32x4 w; w.x = pk2(a[0], a[1]); w.y = pk2(a[2], a[3]); w.z = pk2(b[0], b[1]); w.w = pk2(b[2], b[3]); return w; }
;     __device__ __forceinline__ void operator()(const f32x4 (&acc)[2][2][4][2], const pg8::Unit& u, int wr, int wc, int fr, int fq) const {
;     ...
;         const int sec = pn >> 1, kind = sec % 3, hbase = (sec >= 3) ? 8 : 0;
; #pragma unroll
;         for (int ai = 0; ai < 2; ++ai)
; #pragma unroll
;             for (int m = 0; m < 4; ++m) {
;                 const int t = u.pm * 256 + ai * 128 + wr * 64 + m * 16 + fr; const int b = t >> 11, s = t & 2047;
;                 const float sc = rs[t] * (kind == 0 ? C2 : 1.f);
; #pragma unroll
;                 for (int bj = 0; bj < 2; ++bj) {
;                     const int cc = (pn & 1) * 256 + bj * 128 + wc * 32 + fq * 8, hh = hbase + (cc >> 6), d0 = cc & 63;
;                     const f32x4 v0 = acc[ai][bj][m][0] * sc, v1 = acc[ai][bj][m][1] * sc;
;                     if (kind < 2) { bf16_t* dst = (kind == 0 ? QH : KH) + ((size_t)(b * 16 + hh) * 2048 + s) * 64 + d0; *(u32x4*)dst = pack8(v0, v1); }
;                     else { bf16_t* dst = VT + ((size_t)(b * 16 + hh) * 64 + d0) * 2048 + s;
;                         dst[0 * 2048] = (bf16_t)f2bf(v0[0]); dst[1 * 2048] = (bf16_t)f2bf(v0[1]); dst[2 * 2048] = (bf16_t)f2bf(v0[2]); dst[3 * 2048] = (bf16_t)f2bf(v0[3]);
;                         dst[4 * 2048] = (bf16_t)f2bf(v1[0]); dst[5 * 2048] = (bf16_t)f2bf(v1[1]); dst[6 * 2048] = (bf16_t)f2bf(v1[2]); dst[7 * 2048] = (bf16_t)f2bf(v1[3]); }
.LBB0_384:
	s_ashr_i32 s6, s8, 1
	s_mul_hi_i32 s7, s6, 0x55555556
	s_lshr_b32 s9, s7, 31
	s_add_i32 s7, s7, s9
	s_mul_i32 s7, s7, 3
	s_sub_i32 s9, s6, s7
	s_cmp_gt_i32 s6, 2
	s_cselect_b32 s23, 8, 0
	s_cmp_eq_u32 s9, 0
	s_cselect_b64 s[6:7], -1, 0
	s_lshl_b32 s8, s8, 8
	s_and_b32 s8, s8, 0x100
	s_or_b32 s29, s8, s0
	s_cmp_gt_i32 s9, 1
	s_cselect_b64 s[36:37], -1, 0
	s_lshl_b32 s21, s28, 8
	s_add_i32 s21, s21, s55
	v_or_b32_e32 v152, s21, v139
	v_ashrrev_i32_e32 v153, 31, v152
	v_lshl_add_u64 v[150:151], v[152:153], 2, s[92:93]
	v_mov_b64_e32 v[186:187], v[150:151]
	global_load_dword v150, v[150:151], off
	global_load_dword v188, v[186:187], off offset:64
	global_load_dword v189, v[186:187], off offset:128
	global_load_dword v190, v[186:187], off offset:192
	global_load_dword v191, v[186:187], off offset:512
	global_load_dword v192, v[186:187], off offset:576
	global_load_dword v193, v[186:187], off offset:640
	global_load_dword v194, v[186:187], off offset:704
	s_lshr_b32 s29, s29, 6
	s_or_b32 s23, s29, s23
	s_ashr_i32 s29, s21, 7
	s_and_b32 s33, s29, -16
	s_or_b32 s30, s23, s33
	v_cndmask_b32_e64 v153, 1.0, v173, s[6:7]
	s_ashr_i32 s31, s30, 31
	v_bitop3_b32 v136, s21, v174, v139 bitop3:0xc8
	s_lshl_b64 s[30:31], s[30:31], 18
	s_mov_b64 s[8:9], -1
	s_and_b64 vcc, exec, s[36:37]
	v_lshlrev_b32_e32 v156, 1, v136
	v_lshl_add_u64 v[154:155], v[140:141], 0, s[30:31]
	s_waitcnt vmcnt(0)
	v_mul_f32_e32 v158, v153, v150
	v_pk_mul_f32 v[160:161], v[62:63], v[158:159] op_sel_hi:[1,0]
	v_pk_mul_f32 v[164:165], v[60:61], v[158:159] op_sel_hi:[1,0]
	v_pk_mul_f32 v[162:163], v[58:59], v[158:159] op_sel_hi:[1,0]
	v_pk_mul_f32 v[166:167], v[56:57], v[158:159] op_sel_hi:[1,0]
	s_cbranch_vccz .LBB0_386
	v_mov_b32_e32 v157, v137
	v_lshl_add_u64 v[150:151], v[154:155], 0, v[156:157]
	v_bfe_u32 v157, v164, 16, 1
	v_add3_u32 v157, v164, v157, s63
	global_store_short_d16_hi v[150:151], v157, off
	v_bfe_u32 v157, v165, 16, 1
	v_add_co_u32_e32 v176, vcc, 0x1000, v150
	v_add3_u32 v157, v165, v157, s63
	s_nop 0
	v_addc_co_u32_e32 v177, vcc, 0, v151, vcc
	global_store_short_d16_hi v[176:177], v157, off
	v_bfe_u32 v157, v160, 16, 1
	v_add_co_u32_e32 v176, vcc, s64, v150
	v_add3_u32 v157, v160, v157, s63
	s_nop 0
	v_addc_co_u32_e32 v177, vcc, 0, v151, vcc
	global_store_short_d16_hi v[176:177], v157, off offset:-4096
	v_bfe_u32 v157, v161, 16, 1
	v_add3_u32 v157, v161, v157, s63
	global_store_short_d16_hi v[176:177], v157, off
	v_bfe_u32 v157, v166, 16, 1
	v_add_co_u32_e32 v176, vcc, s52, v150
	v_add3_u32 v157, v166, v157, s63
	s_nop 0
	v_addc_co_u32_e32 v177, vcc, 0, v151, vcc
	global_store_short_d16_hi v[176:177], v157, off
	v_bfe_u32 v157, v167, 16, 1
	v_add_co_u32_e32 v176, vcc, 0x5000, v150
	v_add3_u32 v157, v167, v157, s63
	s_nop 0
	v_addc_co_u32_e32 v177, vcc, 0, v151, vcc
	global_store_short_d16_hi v[176:177], v157, off
	v_bfe_u32 v157, v162, 16, 1
	v_add_co_u32_e32 v176, vcc, 0x6000, v150
	v_add3_u32 v157, v162, v157, s63
	s_nop 0
	v_addc_co_u32_e32 v177, vcc, 0, v151, vcc
	global_store_short_d16_hi v[176:177], v157, off
	v_bfe_u32 v157, v163, 16, 1
	v_add_co_u32_e32 v150, vcc, 0x7000, v150
	v_add3_u32 v157, v163, v157, s63
	s_nop 0
	v_addc_co_u32_e32 v151, vcc, 0, v151, vcc
	global_store_short_d16_hi v[150:151], v157, off
	s_mov_b64 s[8:9], 0

; __device__ __forceinline__ unsigned f2bf(float f) { unsigned u = __builtin_bit_cast(unsigned, f); return (u + 0x7fffu + ((u >> 16) & 1u)) >> 16; }
; __device__ __forceinline__ u32x4 pack8(f32x4 a, f32x4 b) { u32x4 w; w.x = pk2(a[0], a[1]); w.y = pk2(a[2], a[3]); w.z = pk2(b[0], b[1]); w.w = pk2(b[2], b[3]); return w; }
;     __device__ __forceinline__ void operator()(const f32x4 (&acc)[2][2][4][2], const pg8::Unit& u, int wr, int wc, int fr, int fq) const {
;     ...
;                 const int t = u.pm * 256 + ai * 128 + wr * 64 + m * 16 + fr; const int b = t >> 11, s = t & 2047;
;                 const float sc = rs[t] * (kind == 0 ? C2 : 1.f);
; #pragma unroll
;                 for (int bj = 0; bj < 2; ++bj) {
;                     const int cc = (pn & 1) * 256 + bj * 128 + wc * 32 + fq * 8, hh = hbase + (cc >> 6), d0 = cc & 63;
;                     const f32x4 v0 = acc[ai][bj][m][0] * sc, v1 = acc[ai][bj][m][1] * sc;
;                     if (kind < 2) { bf16_t* dst = (kind == 0 ? QH : KH) + ((size_t)(b * 16 + hh) * 2048 + s) * 64 + d0; *(u32x4*)dst = pack8(v0, v1); }
;                     else { bf16_t* dst = VT + ((size_t)(b * 16 + hh) * 64 + d0) * 2048 + s;
;                         dst[0 * 2048] = (bf16_t)f2bf(v0[0]); dst[1 * 2048] = (bf16_t)f2bf(v0[1]); dst[2 * 2048] = (bf16_t)f2bf(v0[2]); dst[3 * 2048] = (bf16_t)f2bf(v0[3]);
;                         dst[4 * 2048] = (bf16_t)f2bf(v1[0]); dst[5 * 2048] = (bf16_t)f2bf(v1[1]); dst[6 * 2048] = (bf16_t)f2bf(v1[2]); dst[7 * 2048] = (bf16_t)f2bf(v1[3]); }
.LBB0_392:
	v_or_b32_e32 v122, 16, v152
	v_ashrrev_i32_e32 v123, 31, v122
	v_lshl_add_u64 v[122:123], v[122:123], 2, s[92:93]
	v_mov_b32_e32 v123, v188
	v_bitop3_b32 v122, v152, s65, 16 bitop3:0xc8
	s_mov_b64 s[36:37], -1
	s_and_b64 vcc, exec, s[8:9]
	v_lshlrev_b32_e32 v136, 1, v122
	v_mul_f32_e32 v124, v153, v123
	v_pk_mul_f32 v[126:127], v[54:55], v[124:125] op_sel_hi:[1,0]
	v_pk_mul_f32 v[158:159], v[52:53], v[124:125] op_sel_hi:[1,0]
	v_pk_mul_f32 v[156:157], v[50:51], v[124:125] op_sel_hi:[1,0]
	v_pk_mul_f32 v[160:161], v[48:49], v[124:125] op_sel_hi:[1,0]
	s_cbranch_vccnz .LBB0_394
	v_bfe_u32 v123, v158, 16, 1
	v_lshl_add_u64 v[162:163], v[154:155], 0, v[136:137]
	v_add3_u32 v123, v158, v123, s63
	global_store_short_d16_hi v[162:163], v123, off
	v_bfe_u32 v123, v159, 16, 1
	v_add_co_u32_e32 v164, vcc, 0x1000, v162
	v_add3_u32 v123, v159, v123, s63
	s_nop 0
	v_addc_co_u32_e32 v165, vcc, 0, v163, vcc
	global_store_short_d16_hi v[164:165], v123, off
	v_bfe_u32 v123, v126, 16, 1
	v_add_co_u32_e32 v164, vcc, s64, v162
	v_add3_u32 v123, v126, v123, s63
	s_nop 0
	v_addc_co_u32_e32 v165, vcc, 0, v163, vcc
	global_store_short_d16_hi v[164:165], v123, off offset:-4096
	v_bfe_u32 v123, v127, 16, 1
	v_add3_u32 v123, v127, v123, s63
	global_store_short_d16_hi v[164:165], v123, off
	v_bfe_u32 v123, v160, 16, 1
	v_add_co_u32_e32 v164, vcc, s52, v162
	v_add3_u32 v123, v160, v123, s63
	s_nop 0
	v_addc_co_u32_e32 v165, vcc, 0, v163, vcc
	global_store_short_d16_hi v[164:165], v123, off
	v_bfe_u32 v123, v161, 16, 1
	v_add_co_u32_e32 v164, vcc, 0x5000, v162
	v_add3_u32 v123, v161, v123, s63
	s_nop 0
	v_addc_co_u32_e32 v165, vcc, 0, v163, vcc
	global_store_short_d16_hi v[164:165], v123, off
	v_bfe_u32 v123, v156, 16, 1
	v_add_co_u32_e32 v164, vcc, 0x6000, v162
	v_add3_u32 v123, v156, v123, s63
	s_nop 0
	v_addc_co_u32_e32 v165, vcc, 0, v163, vcc
	global_store_short_d16_hi v[164:165], v123, off
	v_bfe_u32 v123, v157, 16, 1
	v_add_co_u32_e32 v162, vcc, 0x7000, v162
	v_add3_u32 v123, v157, v123, s63
	s_nop 0
	v_addc_co_u32_e32 v163, vcc, 0, v163, vcc
	s_mov_b64 s[36:37], 0
	global_store_short_d16_hi v[162:163], v123, off

; __device__ __forceinline__ unsigned f2bf(float f) { unsigned u = __builtin_bit_cast(unsigned, f); return (u + 0x7fffu + ((u >> 16) & 1u)) >> 16; }
; __device__ __forceinline__ u32x4 pack8(f32x4 a, f32x4 b) { u32x4 w; w.x = pk2(a[0], a[1]); w.y = pk2(a[2], a[3]); w.z = pk2(b[0], b[1]); w.w = pk2(b[2], b[3]); return w; }
;     __device__ __forceinline__ void operator()(const f32x4 (&acc)[2][2][4][2], const pg8::Unit& u, int wr, int wc, int fr, int fq) const {
;     ...
;                 const int t = u.pm * 256 + ai * 128 + wr * 64 + m * 16 + fr; const int b = t >> 11, s = t & 2047;
;                 const float sc = rs[t] * (kind == 0 ? C2 : 1.f);
; #pragma unroll
;                 for (int bj = 0; bj < 2; ++bj) {
;                     const int cc = (pn & 1) * 256 + bj * 128 + wc * 32 + fq * 8, hh = hbase + (cc >> 6), d0 = cc & 63;
;                     const f32x4 v0 = acc[ai][bj][m][0] * sc, v1 = acc[ai][bj][m][1] * sc;
;                     if (kind < 2) { bf16_t* dst = (kind == 0 ? QH : KH) + ((size_t)(b * 16 + hh) * 2048 + s) * 64 + d0; *(u32x4*)dst = pack8(v0, v1); }
;                     else { bf16_t* dst = VT + ((size_t)(b * 16 + hh) * 64 + d0) * 2048 + s;
;                         dst[0 * 2048] = (bf16_t)f2bf(v0[0]); dst[1 * 2048] = (bf16_t)f2bf(v0[1]); dst[2 * 2048] = (bf16_t)f2bf(v0[2]); dst[3 * 2048] = (bf16_t)f2bf(v0[3]);
;                         dst[4 * 2048] = (bf16_t)f2bf(v1[0]); dst[5 * 2048] = (bf16_t)f2bf(v1[1]); dst[6 * 2048] = (bf16_t)f2bf(v1[2]); dst[7 * 2048] = (bf16_t)f2bf(v1[3]); }
.LBB0_400:
	v_or_b32_e32 v112, 32, v152
	v_ashrrev_i32_e32 v113, 31, v112
	v_lshl_add_u64 v[112:113], v[112:113], 2, s[92:93]
	v_mov_b32_e32 v113, v189
	v_bitop3_b32 v112, v152, s66, 32 bitop3:0xc8
	s_mov_b64 s[36:37], -1
	s_and_b64 vcc, exec, s[8:9]
	v_lshlrev_b32_e32 v136, 1, v112
	v_mul_f32_e32 v114, v153, v113
	v_pk_mul_f32 v[116:117], v[46:47], v[114:115] op_sel_hi:[1,0]
	v_pk_mul_f32 v[122:123], v[44:45], v[114:115] op_sel_hi:[1,0]
	v_pk_mul_f32 v[118:119], v[42:43], v[114:115] op_sel_hi:[1,0]
	v_pk_mul_f32 v[124:125], v[40:41], v[114:115] op_sel_hi:[1,0]
	s_cbranch_vccnz .LBB0_402
	v_bfe_u32 v113, v122, 16, 1
	v_lshl_add_u64 v[126:127], v[154:155], 0, v[136:137]
	v_add3_u32 v113, v122, v113, s63
	global_store_short_d16_hi v[126:127], v113, off
	v_bfe_u32 v113, v123, 16, 1
	v_add_co_u32_e32 v156, vcc, 0x1000, v126
	v_add3_u32 v113, v123, v113, s63
	s_nop 0
	v_addc_co_u32_e32 v157, vcc, 0, v127, vcc
	global_store_short_d16_hi v[156:157], v113, off
	v_bfe_u32 v113, v116, 16, 1
	v_add_co_u32_e32 v156, vcc, s64, v126
	v_add3_u32 v113, v116, v113, s63
	s_nop 0
	v_addc_co_u32_e32 v157, vcc, 0, v127, vcc
	global_store_short_d16_hi v[156:157], v113, off offset:-4096
	v_bfe_u32 v113, v117, 16, 1
	v_add3_u32 v113, v117, v113, s63
	global_store_short_d16_hi v[156:157], v113, off
	v_bfe_u32 v113, v124, 16, 1
	v_add_co_u32_e32 v156, vcc, s52, v126
	v_add3_u32 v113, v124, v113, s63
	s_nop 0
	v_addc_co_u32_e32 v157, vcc, 0, v127, vcc
	global_store_short_d16_hi v[156:157], v113, off
	v_bfe_u32 v113, v125, 16, 1
	v_add_co_u32_e32 v156, vcc, 0x5000, v126
	v_add3_u32 v113, v125, v113, s63
	s_nop 0
	v_addc_co_u32_e32 v157, vcc, 0, v127, vcc
	global_store_short_d16_hi v[156:157], v113, off
	v_bfe_u32 v113, v118, 16, 1
	v_add_co_u32_e32 v156, vcc, 0x6000, v126
	v_add3_u32 v113, v118, v113, s63
	s_nop 0
	v_addc_co_u32_e32 v157, vcc, 0, v127, vcc
	global_store_short_d16_hi v[156:157], v113, off
	v_bfe_u32 v113, v119, 16, 1
	v_add_co_u32_e32 v126, vcc, 0x7000, v126
	v_add3_u32 v113, v119, v113, s63
	s_nop 0
	v_addc_co_u32_e32 v127, vcc, 0, v127, vcc
	s_mov_b64 s[36:37], 0
	global_store_short_d16_hi v[126:127], v113, off

; __device__ __forceinline__ unsigned f2bf(float f) { unsigned u = __builtin_bit_cast(unsigned, f); return (u + 0x7fffu + ((u >> 16) & 1u)) >> 16; }
; __device__ __forceinline__ u32x4 pack8(f32x4 a, f32x4 b) { u32x4 w; w.x = pk2(a[0], a[1]); w.y = pk2(a[2], a[3]); w.z = pk2(b[0], b[1]); w.w = pk2(b[2], b[3]); return w; }
;     __device__ __forceinline__ void operator()(const f32x4 (&acc)[2][2][4][2], const pg8::Unit& u, int wr, int wc, int fr, int fq) const {
;     ...
;                 const int t = u.pm * 256 + ai * 128 + wr * 64 + m * 16 + fr; const int b = t >> 11, s = t & 2047;
;                 const float sc = rs[t] * (kind == 0 ? C2 : 1.f);
; #pragma unroll
;                 for (int bj = 0; bj < 2; ++bj) {
;                     const int cc = (pn & 1) * 256 + bj * 128 + wc * 32 + fq * 8, hh = hbase + (cc >> 6), d0 = cc & 63;
;                     const f32x4 v0 = acc[ai][bj][m][0] * sc, v1 = acc[ai][bj][m][1] * sc;
;                     if (kind < 2) { bf16_t* dst = (kind == 0 ? QH : KH) + ((size_t)(b * 16 + hh) * 2048 + s) * 64 + d0; *(u32x4*)dst = pack8(v0, v1); }
;                     else { bf16_t* dst = VT + ((size_t)(b * 16 + hh) * 64 + d0) * 2048 + s;
;                         dst[0 * 2048] = (bf16_t)f2bf(v0[0]); dst[1 * 2048] = (bf16_t)f2bf(v0[1]); dst[2 * 2048] = (bf16_t)f2bf(v0[2]); dst[3 * 2048] = (bf16_t)f2bf(v0[3]);
;                         dst[4 * 2048] = (bf16_t)f2bf(v1[0]); dst[5 * 2048] = (bf16_t)f2bf(v1[1]); dst[6 * 2048] = (bf16_t)f2bf(v1[2]); dst[7 * 2048] = (bf16_t)f2bf(v1[3]); }
.LBB0_408:
	v_or_b32_e32 v104, 48, v152
	v_ashrrev_i32_e32 v105, 31, v104
	v_lshl_add_u64 v[104:105], v[104:105], 2, s[92:93]
	v_mov_b32_e32 v105, v190
	v_bitop3_b32 v104, v152, s67, 48 bitop3:0xc8
	s_mov_b64 s[36:37], -1
	s_and_b64 vcc, exec, s[8:9]
	v_lshlrev_b32_e32 v136, 1, v104
	v_mul_f32_e32 v106, v153, v105
	v_pk_mul_f32 v[108:109], v[38:39], v[106:107] op_sel_hi:[1,0]
	v_pk_mul_f32 v[112:113], v[36:37], v[106:107] op_sel_hi:[1,0]
	v_pk_mul_f32 v[110:111], v[34:35], v[106:107] op_sel_hi:[1,0]
	v_pk_mul_f32 v[114:115], v[32:33], v[106:107] op_sel_hi:[1,0]
	s_cbranch_vccnz .LBB0_410
	v_bfe_u32 v105, v112, 16, 1
	v_lshl_add_u64 v[116:117], v[154:155], 0, v[136:137]
	v_add3_u32 v105, v112, v105, s63
	global_store_short_d16_hi v[116:117], v105, off
	v_bfe_u32 v105, v113, 16, 1
	v_add_co_u32_e32 v118, vcc, 0x1000, v116
	v_add3_u32 v105, v113, v105, s63
	s_nop 0
	v_addc_co_u32_e32 v119, vcc, 0, v117, vcc
	global_store_short_d16_hi v[118:119], v105, off
	v_bfe_u32 v105, v108, 16, 1
	v_add_co_u32_e32 v118, vcc, s64, v116
	v_add3_u32 v105, v108, v105, s63
	s_nop 0
	v_addc_co_u32_e32 v119, vcc, 0, v117, vcc
	global_store_short_d16_hi v[118:119], v105, off offset:-4096
	v_bfe_u32 v105, v109, 16, 1
	v_add3_u32 v105, v109, v105, s63
	global_store_short_d16_hi v[118:119], v105, off
	v_bfe_u32 v105, v114, 16, 1
	v_add_co_u32_e32 v118, vcc, s52, v116
	v_add3_u32 v105, v114, v105, s63
	s_nop 0
	v_addc_co_u32_e32 v119, vcc, 0, v117, vcc
	global_store_short_d16_hi v[118:119], v105, off
	v_bfe_u32 v105, v115, 16, 1
	v_add_co_u32_e32 v118, vcc, 0x5000, v116
	v_add3_u32 v105, v115, v105, s63
	s_nop 0
	v_addc_co_u32_e32 v119, vcc, 0, v117, vcc
	global_store_short_d16_hi v[118:119], v105, off
	v_bfe_u32 v105, v110, 16, 1
	v_add_co_u32_e32 v118, vcc, 0x6000, v116
	v_add3_u32 v105, v110, v105, s63
	s_nop 0
	v_addc_co_u32_e32 v119, vcc, 0, v117, vcc
	global_store_short_d16_hi v[118:119], v105, off
	v_bfe_u32 v105, v111, 16, 1
	v_add_co_u32_e32 v116, vcc, 0x7000, v116
	v_add3_u32 v105, v111, v105, s63
	s_nop 0
	v_addc_co_u32_e32 v117, vcc, 0, v117, vcc
	s_mov_b64 s[36:37], 0
	global_store_short_d16_hi v[116:117], v105, off

; __device__ __forceinline__ unsigned f2bf(float f) { unsigned u = __builtin_bit_cast(unsigned, f); return (u + 0x7fffu + ((u >> 16) & 1u)) >> 16; }
; __device__ __forceinline__ u32x4 pack8(f32x4 a, f32x4 b) { u32x4 w; w.x = pk2(a[0], a[1]); w.y = pk2(a[2], a[3]); w.z = pk2(b[0], b[1]); w.w = pk2(b[2], b[3]); return w; }
;     __device__ __forceinline__ void operator()(const f32x4 (&acc)[2][2][4][2], const pg8::Unit& u, int wr, int wc, int fr, int fq) const {
;     ...
;                 const int t = u.pm * 256 + ai * 128 + wr * 64 + m * 16 + fr; const int b = t >> 11, s = t & 2047;
;                 const float sc = rs[t] * (kind == 0 ? C2 : 1.f);
; #pragma unroll
;                 for (int bj = 0; bj < 2; ++bj) {
;                     const int cc = (pn & 1) * 256 + bj * 128 + wc * 32 + fq * 8, hh = hbase + (cc >> 6), d0 = cc & 63;
;                     const f32x4 v0 = acc[ai][bj][m][0] * sc, v1 = acc[ai][bj][m][1] * sc;
;                     if (kind < 2) { bf16_t* dst = (kind == 0 ? QH : KH) + ((size_t)(b * 16 + hh) * 2048 + s) * 64 + d0; *(u32x4*)dst = pack8(v0, v1); }
;                     else { bf16_t* dst = VT + ((size_t)(b * 16 + hh) * 64 + d0) * 2048 + s;
;                         dst[0 * 2048] = (bf16_t)f2bf(v0[0]); dst[1 * 2048] = (bf16_t)f2bf(v0[1]); dst[2 * 2048] = (bf16_t)f2bf(v0[2]); dst[3 * 2048] = (bf16_t)f2bf(v0[3]);
;                         dst[4 * 2048] = (bf16_t)f2bf(v1[0]); dst[5 * 2048] = (bf16_t)f2bf(v1[1]); dst[6 * 2048] = (bf16_t)f2bf(v1[2]); dst[7 * 2048] = (bf16_t)f2bf(v1[3]); }
.LBB0_416:
	s_addk_i32 s21, 0x80
	v_or_b32_e32 v96, s21, v139
	v_ashrrev_i32_e32 v97, 31, v96
	v_lshl_add_u64 v[98:99], v[96:97], 2, s[92:93]
	v_mov_b32_e32 v100, v191
	v_bitop3_b32 v97, s21, v174, v139 bitop3:0xc8
	s_ashr_i32 s21, s21, 7
	s_and_b32 s21, s21, -16
	s_or_b32 s30, s23, s21
	s_ashr_i32 s31, s30, 31
	s_lshl_b64 s[30:31], s[30:31], 18
	s_mov_b64 s[34:35], -1
	s_and_b64 vcc, exec, s[8:9]
	v_lshl_add_u64 v[98:99], v[140:141], 0, s[30:31]
	v_lshlrev_b32_e32 v136, 1, v97
	v_mul_f32_e32 v102, v153, v100
	v_pk_mul_f32 v[104:105], v[30:31], v[102:103] op_sel_hi:[1,0]
	v_pk_mul_f32 v[108:109], v[28:29], v[102:103] op_sel_hi:[1,0]
	v_pk_mul_f32 v[106:107], v[26:27], v[102:103] op_sel_hi:[1,0]
	v_pk_mul_f32 v[110:111], v[24:25], v[102:103] op_sel_hi:[1,0]
	s_cbranch_vccnz .LBB0_418
	v_bfe_u32 v103, v108, 16, 1
	v_lshl_add_u64 v[100:101], v[98:99], 0, v[136:137]
	v_add3_u32 v103, v108, v103, s63
	global_store_short_d16_hi v[100:101], v103, off
	v_bfe_u32 v103, v109, 16, 1
	v_add_co_u32_e32 v112, vcc, 0x1000, v100
	v_add3_u32 v103, v109, v103, s63
	s_nop 0
	v_addc_co_u32_e32 v113, vcc, 0, v101, vcc
	global_store_short_d16_hi v[112:113], v103, off
	v_bfe_u32 v103, v104, 16, 1
	v_add_co_u32_e32 v112, vcc, s64, v100
	v_add3_u32 v103, v104, v103, s63
	s_nop 0
	v_addc_co_u32_e32 v113, vcc, 0, v101, vcc
	global_store_short_d16_hi v[112:113], v103, off offset:-4096
	v_bfe_u32 v103, v105, 16, 1
	v_add3_u32 v103, v105, v103, s63
	global_store_short_d16_hi v[112:113], v103, off
	v_bfe_u32 v103, v110, 16, 1
	v_add_co_u32_e32 v112, vcc, s52, v100
	v_add3_u32 v103, v110, v103, s63
	s_nop 0
	v_addc_co_u32_e32 v113, vcc, 0, v101, vcc
	global_store_short_d16_hi v[112:113], v103, off
	v_bfe_u32 v103, v111, 16, 1
	v_add_co_u32_e32 v112, vcc, 0x5000, v100
	v_add3_u32 v103, v111, v103, s63
	s_nop 0
	v_addc_co_u32_e32 v113, vcc, 0, v101, vcc
	global_store_short_d16_hi v[112:113], v103, off
	v_bfe_u32 v103, v106, 16, 1
	v_add_co_u32_e32 v112, vcc, 0x6000, v100
	v_add3_u32 v103, v106, v103, s63
	s_nop 0
	v_addc_co_u32_e32 v113, vcc, 0, v101, vcc
	global_store_short_d16_hi v[112:113], v103, off
	v_bfe_u32 v103, v107, 16, 1
	v_add_co_u32_e32 v100, vcc, 0x7000, v100
	v_add3_u32 v103, v107, v103, s63
	s_nop 0
	v_addc_co_u32_e32 v101, vcc, 0, v101, vcc
	s_mov_b64 s[34:35], 0
	global_store_short_d16_hi v[100:101], v103, off

; __device__ __forceinline__ unsigned f2bf(float f) { unsigned u = __builtin_bit_cast(unsigned, f); return (u + 0x7fffu + ((u >> 16) & 1u)) >> 16; }
; __device__ __forceinline__ u32x4 pack8(f32x4 a, f32x4 b) { u32x4 w; w.x = pk2(a[0], a[1]); w.y = pk2(a[2], a[3]); w.z = pk2(b[0], b[1]); w.w = pk2(b[2], b[3]); return w; }
;     __device__ __forceinline__ void operator()(const f32x4 (&acc)[2][2][4][2], const pg8::Unit& u, int wr, int wc, int fr, int fq) const {
;     ...
;                 const int t = u.pm * 256 + ai * 128 + wr * 64 + m * 16 + fr; const int b = t >> 11, s = t & 2047;
;                 const float sc = rs[t] * (kind == 0 ? C2 : 1.f);
; #pragma unroll
;                 for (int bj = 0; bj < 2; ++bj) {
;                     const int cc = (pn & 1) * 256 + bj * 128 + wc * 32 + fq * 8, hh = hbase + (cc >> 6), d0 = cc & 63;
;                     const f32x4 v0 = acc[ai][bj][m][0] * sc, v1 = acc[ai][bj][m][1] * sc;
;                     if (kind < 2) { bf16_t* dst = (kind == 0 ? QH : KH) + ((size_t)(b * 16 + hh) * 2048 + s) * 64 + d0; *(u32x4*)dst = pack8(v0, v1); }
;                     else { bf16_t* dst = VT + ((size_t)(b * 16 + hh) * 64 + d0) * 2048 + s;
;                         dst[0 * 2048] = (bf16_t)f2bf(v0[0]); dst[1 * 2048] = (bf16_t)f2bf(v0[1]); dst[2 * 2048] = (bf16_t)f2bf(v0[2]); dst[3 * 2048] = (bf16_t)f2bf(v0[3]);
;                         dst[4 * 2048] = (bf16_t)f2bf(v1[0]); dst[5 * 2048] = (bf16_t)f2bf(v1[1]); dst[6 * 2048] = (bf16_t)f2bf(v1[2]); dst[7 * 2048] = (bf16_t)f2bf(v1[3]); }
.LBB0_424:
	v_or_b32_e32 v90, 16, v96
	v_ashrrev_i32_e32 v91, 31, v90
	v_lshl_add_u64 v[90:91], v[90:91], 2, s[92:93]
	v_mov_b32_e32 v91, v192
	v_bitop3_b32 v90, v96, s65, 16 bitop3:0xc8
	s_mov_b64 s[36:37], -1
	s_and_b64 vcc, exec, s[8:9]
	v_lshlrev_b32_e32 v136, 1, v90
	v_mul_f32_e32 v92, v153, v91
	v_pk_mul_f32 v[94:95], v[22:23], v[92:93] op_sel_hi:[1,0]
	v_pk_mul_f32 v[102:103], v[20:21], v[92:93] op_sel_hi:[1,0]
	v_pk_mul_f32 v[100:101], v[18:19], v[92:93] op_sel_hi:[1,0]
	v_pk_mul_f32 v[104:105], v[16:17], v[92:93] op_sel_hi:[1,0]
	s_cbranch_vccnz .LBB0_426
	v_bfe_u32 v91, v102, 16, 1
	v_lshl_add_u64 v[106:107], v[98:99], 0, v[136:137]
	v_add3_u32 v91, v102, v91, s63
	global_store_short_d16_hi v[106:107], v91, off
	v_bfe_u32 v91, v103, 16, 1
	v_add_co_u32_e32 v108, vcc, 0x1000, v106
	v_add3_u32 v91, v103, v91, s63
	s_nop 0
	v_addc_co_u32_e32 v109, vcc, 0, v107, vcc
	global_store_short_d16_hi v[108:109], v91, off
	v_bfe_u32 v91, v94, 16, 1
	v_add_co_u32_e32 v108, vcc, s64, v106
	v_add3_u32 v91, v94, v91, s63
	s_nop 0
	v_addc_co_u32_e32 v109, vcc, 0, v107, vcc
	global_store_short_d16_hi v[108:109], v91, off offset:-4096
	v_bfe_u32 v91, v95, 16, 1
	v_add3_u32 v91, v95, v91, s63
	global_store_short_d16_hi v[108:109], v91, off
	v_bfe_u32 v91, v104, 16, 1
	v_add_co_u32_e32 v108, vcc, s52, v106
	v_add3_u32 v91, v104, v91, s63
	s_nop 0
	v_addc_co_u32_e32 v109, vcc, 0, v107, vcc
	global_store_short_d16_hi v[108:109], v91, off
	v_bfe_u32 v91, v105, 16, 1
	v_add_co_u32_e32 v108, vcc, 0x5000, v106
	v_add3_u32 v91, v105, v91, s63
	s_nop 0
	v_addc_co_u32_e32 v109, vcc, 0, v107, vcc
	global_store_short_d16_hi v[108:109], v91, off
	v_bfe_u32 v91, v100, 16, 1
	v_add_co_u32_e32 v108, vcc, 0x6000, v106
	v_add3_u32 v91, v100, v91, s63
	s_nop 0
	v_addc_co_u32_e32 v109, vcc, 0, v107, vcc
	global_store_short_d16_hi v[108:109], v91, off
	v_bfe_u32 v91, v101, 16, 1
	v_add_co_u32_e32 v106, vcc, 0x7000, v106
	v_add3_u32 v91, v101, v91, s63
	s_nop 0
	v_addc_co_u32_e32 v107, vcc, 0, v107, vcc
	s_mov_b64 s[36:37], 0
	global_store_short_d16_hi v[106:107], v91, off

; __device__ __forceinline__ unsigned f2bf(float f) { unsigned u = __builtin_bit_cast(unsigned, f); return (u + 0x7fffu + ((u >> 16) & 1u)) >> 16; }
; __device__ __forceinline__ u32x4 pack8(f32x4 a, f32x4 b) { u32x4 w; w.x = pk2(a[0], a[1]); w.y = pk2(a[2], a[3]); w.z = pk2(b[0], b[1]); w.w = pk2(b[2], b[3]); return w; }
;     __device__ __forceinline__ void operator()(const f32x4 (&acc)[2][2][4][2], const pg8::Unit& u, int wr, int wc, int fr, int fq) const {
;     ...
;                 const int t = u.pm * 256 + ai * 128 + wr * 64 + m * 16 + fr; const int b = t >> 11, s = t & 2047;
;                 const float sc = rs[t] * (kind == 0 ? C2 : 1.f);
; #pragma unroll
;                 for (int bj = 0; bj < 2; ++bj) {
;                     const int cc = (pn & 1) * 256 + bj * 128 + wc * 32 + fq * 8, hh = hbase + (cc >> 6), d0 = cc & 63;
;                     const f32x4 v0 = acc[ai][bj][m][0] * sc, v1 = acc[ai][bj][m][1] * sc;
;                     if (kind < 2) { bf16_t* dst = (kind == 0 ? QH : KH) + ((size_t)(b * 16 + hh) * 2048 + s) * 64 + d0; *(u32x4*)dst = pack8(v0, v1); }
;                     else { bf16_t* dst = VT + ((size_t)(b * 16 + hh) * 64 + d0) * 2048 + s;
;                         dst[0 * 2048] = (bf16_t)f2bf(v0[0]); dst[1 * 2048] = (bf16_t)f2bf(v0[1]); dst[2 * 2048] = (bf16_t)f2bf(v0[2]); dst[3 * 2048] = (bf16_t)f2bf(v0[3]);
;                         dst[4 * 2048] = (bf16_t)f2bf(v1[0]); dst[5 * 2048] = (bf16_t)f2bf(v1[1]); dst[6 * 2048] = (bf16_t)f2bf(v1[2]); dst[7 * 2048] = (bf16_t)f2bf(v1[3]); }
.LBB0_432:
	v_or_b32_e32 v80, 32, v96
	v_ashrrev_i32_e32 v81, 31, v80
	v_lshl_add_u64 v[80:81], v[80:81], 2, s[92:93]
	v_mov_b32_e32 v81, v193
	v_bitop3_b32 v80, v96, s66, 32 bitop3:0xc8
	s_mov_b64 s[36:37], -1
	s_and_b64 vcc, exec, s[8:9]
	v_lshlrev_b32_e32 v136, 1, v80
	v_mul_f32_e32 v82, v153, v81
	v_pk_mul_f32 v[84:85], v[14:15], v[82:83] op_sel_hi:[1,0]
	v_pk_mul_f32 v[90:91], v[12:13], v[82:83] op_sel_hi:[1,0]
	v_pk_mul_f32 v[86:87], v[10:11], v[82:83] op_sel_hi:[1,0]
	v_pk_mul_f32 v[92:93], v[8:9], v[82:83] op_sel_hi:[1,0]
	s_cbranch_vccnz .LBB0_434
	v_bfe_u32 v81, v90, 16, 1
	v_lshl_add_u64 v[94:95], v[98:99], 0, v[136:137]
	v_add3_u32 v81, v90, v81, s63
	global_store_short_d16_hi v[94:95], v81, off
	v_bfe_u32 v81, v91, 16, 1
	v_add_co_u32_e32 v100, vcc, 0x1000, v94
	v_add3_u32 v81, v91, v81, s63
	s_nop 0
	v_addc_co_u32_e32 v101, vcc, 0, v95, vcc
	global_store_short_d16_hi v[100:101], v81, off
	v_bfe_u32 v81, v84, 16, 1
	v_add_co_u32_e32 v100, vcc, s64, v94
	v_add3_u32 v81, v84, v81, s63
	s_nop 0
	v_addc_co_u32_e32 v101, vcc, 0, v95, vcc
	global_store_short_d16_hi v[100:101], v81, off offset:-4096
	v_bfe_u32 v81, v85, 16, 1
	v_add3_u32 v81, v85, v81, s63
	global_store_short_d16_hi v[100:101], v81, off
	v_bfe_u32 v81, v92, 16, 1
	v_add_co_u32_e32 v100, vcc, s52, v94
	v_add3_u32 v81, v92, v81, s63
	s_nop 0
	v_addc_co_u32_e32 v101, vcc, 0, v95, vcc
	global_store_short_d16_hi v[100:101], v81, off
	v_bfe_u32 v81, v93, 16, 1
	v_add_co_u32_e32 v100, vcc, 0x5000, v94
	v_add3_u32 v81, v93, v81, s63
	s_nop 0
	v_addc_co_u32_e32 v101, vcc, 0, v95, vcc
	global_store_short_d16_hi v[100:101], v81, off
	v_bfe_u32 v81, v86, 16, 1
	v_add_co_u32_e32 v100, vcc, 0x6000, v94
	v_add3_u32 v81, v86, v81, s63
	s_nop 0
	v_addc_co_u32_e32 v101, vcc, 0, v95, vcc
	global_store_short_d16_hi v[100:101], v81, off
	v_bfe_u32 v81, v87, 16, 1
	v_add_co_u32_e32 v94, vcc, 0x7000, v94
	v_add3_u32 v81, v87, v81, s63
	s_nop 0
	v_addc_co_u32_e32 v95, vcc, 0, v95, vcc
	s_mov_b64 s[36:37], 0
	global_store_short_d16_hi v[94:95], v81, off

; __device__ __forceinline__ unsigned f2bf(float f) { unsigned u = __builtin_bit_cast(unsigned, f); return (u + 0x7fffu + ((u >> 16) & 1u)) >> 16; }
; __device__ __forceinline__ u32x4 pack8(f32x4 a, f32x4 b) { u32x4 w; w.x = pk2(a[0], a[1]); w.y = pk2(a[2], a[3]); w.z = pk2(b[0], b[1]); w.w = pk2(b[2], b[3]); return w; }
;     __device__ __forceinline__ void operator()(const f32x4 (&acc)[2][2][4][2], const pg8::Unit& u, int wr, int wc, int fr, int fq) const {
;     ...
;                 const int t = u.pm * 256 + ai * 128 + wr * 64 + m * 16 + fr; const int b = t >> 11, s = t & 2047;
;                 const float sc = rs[t] * (kind == 0 ? C2 : 1.f);
; #pragma unroll
;                 for (int bj = 0; bj < 2; ++bj) {
;                     const int cc = (pn & 1) * 256 + bj * 128 + wc * 32 + fq * 8, hh = hbase + (cc >> 6), d0 = cc & 63;
;                     const f32x4 v0 = acc[ai][bj][m][0] * sc, v1 = acc[ai][bj][m][1] * sc;
;                     if (kind < 2) { bf16_t* dst = (kind == 0 ? QH : KH) + ((size_t)(b * 16 + hh) * 2048 + s) * 64 + d0; *(u32x4*)dst = pack8(v0, v1); }
;                     else { bf16_t* dst = VT + ((size_t)(b * 16 + hh) * 64 + d0) * 2048 + s;
;                         dst[0 * 2048] = (bf16_t)f2bf(v0[0]); dst[1 * 2048] = (bf16_t)f2bf(v0[1]); dst[2 * 2048] = (bf16_t)f2bf(v0[2]); dst[3 * 2048] = (bf16_t)f2bf(v0[3]);
;                         dst[4 * 2048] = (bf16_t)f2bf(v1[0]); dst[5 * 2048] = (bf16_t)f2bf(v1[1]); dst[6 * 2048] = (bf16_t)f2bf(v1[2]); dst[7 * 2048] = (bf16_t)f2bf(v1[3]); }
.LBB0_440:
	v_or_b32_e32 v72, 48, v96
	v_ashrrev_i32_e32 v73, 31, v72
	v_lshl_add_u64 v[72:73], v[72:73], 2, s[92:93]
	v_mov_b32_e32 v73, v194
	v_bitop3_b32 v72, v96, s67, 48 bitop3:0xc8
	s_mov_b64 s[36:37], -1
	s_and_b64 vcc, exec, s[8:9]
	v_lshlrev_b32_e32 v136, 1, v72
	v_mul_f32_e32 v74, v153, v73
	v_pk_mul_f32 v[76:77], v[6:7], v[74:75] op_sel_hi:[1,0]
	v_pk_mul_f32 v[80:81], v[4:5], v[74:75] op_sel_hi:[1,0]
	v_pk_mul_f32 v[78:79], v[2:3], v[74:75] op_sel_hi:[1,0]
	v_pk_mul_f32 v[82:83], v[0:1], v[74:75] op_sel_hi:[1,0]
	s_cbranch_vccnz .LBB0_442
	v_bfe_u32 v73, v80, 16, 1
	v_lshl_add_u64 v[84:85], v[98:99], 0, v[136:137]
	v_add3_u32 v73, v80, v73, s63
	global_store_short_d16_hi v[84:85], v73, off
	v_bfe_u32 v73, v81, 16, 1
	v_add_co_u32_e32 v86, vcc, 0x1000, v84
	v_add3_u32 v73, v81, v73, s63
	s_nop 0
	v_addc_co_u32_e32 v87, vcc, 0, v85, vcc
	global_store_short_d16_hi v[86:87], v73, off
	v_bfe_u32 v73, v76, 16, 1
	v_add_co_u32_e32 v86, vcc, s64, v84
	v_add3_u32 v73, v76, v73, s63
	s_nop 0
	v_addc_co_u32_e32 v87, vcc, 0, v85, vcc
	global_store_short_d16_hi v[86:87], v73, off offset:-4096
	v_bfe_u32 v73, v77, 16, 1
	v_add3_u32 v73, v77, v73, s63
	global_store_short_d16_hi v[86:87], v73, off
	v_bfe_u32 v73, v82, 16, 1
	v_add_co_u32_e32 v86, vcc, s52, v84
	v_add3_u32 v73, v82, v73, s63
	s_nop 0
	v_addc_co_u32_e32 v87, vcc, 0, v85, vcc
	global_store_short_d16_hi v[86:87], v73, off
	v_bfe_u32 v73, v83, 16, 1
	v_add_co_u32_e32 v86, vcc, 0x5000, v84
	v_add3_u32 v73, v83, v73, s63
	s_nop 0
	v_addc_co_u32_e32 v87, vcc, 0, v85, vcc
	global_store_short_d16_hi v[86:87], v73, off
	v_bfe_u32 v73, v78, 16, 1
	v_add_co_u32_e32 v86, vcc, 0x6000, v84
	v_add3_u32 v73, v78, v73, s63
	s_nop 0
	v_addc_co_u32_e32 v87, vcc, 0, v85, vcc
	global_store_short_d16_hi v[86:87], v73, off
	v_bfe_u32 v73, v79, 16, 1
	v_add_co_u32_e32 v84, vcc, 0x7000, v84
	v_add3_u32 v73, v79, v73, s63
	s_nop 0
	v_addc_co_u32_e32 v85, vcc, 0, v85, vcc
	s_mov_b64 s[36:37], 0
	global_store_short_d16_hi v[84:85], v73, off

; #define LAS __attribute__((address_space(3)))
; __device__ __forceinline__ void phase_attn_sb_dyn(Frame& F, const bf16_t* QH, const bf16_t* KH, const bf16_t* VT, bf16_t* AO, unsigned* ctr) {
;     LAS int* slotw = (LAS int*)(F.lds + AT_CF + 8192 + 256);
;     for (;;) {
;         __syncthreads();
;         if (F.tid == 0) *slotw = (int)atomicAdd(ctr, 1u);
.LBB0_571:
	v_readlane_b32 s76, v237, 53
	v_readlane_b32 s78, v237, 55
	v_readlane_b32 s79, v237, 56
	s_add_u32 s18, s78, 0x10000
	s_addc_u32 s19, s79, 0
	v_readlane_b32 s74, v237, 44
	s_add_i32 s23, 0, 0x12100
	v_mbcnt_lo_u32_b32 v0, -1, 0
	v_readlane_b32 s77, v237, 54
	s_sub_i32 s22, 7, s74
	s_mov_b32 s21, 0
	v_mov_b32_e32 v129, 0
	v_mov_b32_e32 v138, s23
	s_movk_i32 s24, 0x3ff
	s_movk_i32 s25, 0xffe0
	s_mov_b32 s26, 0xc3480000
	v_mbcnt_hi_u32_b32 v139, -1, v0
	v_mov_b32_e32 v140, 0xff800000
	v_readlane_b32 s72, v237, 57
	v_readlane_b32 s73, v237, 43
	s_mov_b64 s[0:1], exec
	v_readlane_b32 s2, v237, 9
	v_readlane_b32 s3, v237, 10
	s_and_b64 s[2:3], s[0:1], s[2:3]
	s_mov_b64 exec, s[2:3]
	s_cbranch_execz .Lsbq_pre
	v_mov_b32_e32 v180, 1
	global_atomic_add v180, v129, v180, s[18:19] sc0
.Lsbq_pre:
	s_mov_b64 exec, s[0:1]
	s_branch .LBB0_574

; __device__ __forceinline__ int opaque_i(int v) { asm volatile("" : "+v"(v)); return v; }
; __device__ __forceinline__ int pi32(int i) { return (i & ~12) | ((i & 4) << 1) | ((i & 8) >> 1); }
; template <int KIND>
; __device__ __forceinline__ void attn_wave(const bf16_t* Qh, const bf16_t* Kh, const bf16_t* Vth, const int q0, const int lane, const float* CFh, const float slope2, const float* KMh, bf16_t* AOp) {
;     const int r32 = lane & 31, hi = lane >> 5, r32p = pi32(r32), q = q0 + r32;
;     bf16x8 qr[4];
; #pragma unroll
;     for (int d0 = 0; d0 < 4; ++d0) qr[d0] = *(const bf16x8*)(Qh + (size_t)q * 64 + 16 * d0 + 8 * hi);
;     f32x16 O0 = f32x16{}, O1 = f32x16{};
;     float m = -INFINITY, l = 0.f, R = 0.f;
;     bf16x8 kf[4], kfn[4], vf[2][2];
;     const int nt = q0 / 32 + 1;
; __device__ __forceinline__ void phase_attn_sb_dyn(Frame& F, const bf16_t* QH, const bf16_t* KH, const bf16_t* VT, bf16_t* AO, unsigned* ctr) {
;     ...
;     for (;;) {
;         __syncthreads();
;         if (F.tid == 0) *slotw = (int)atomicAdd(ctr, 1u);
;         __syncthreads();
;         const int k = *slotw; if (k >= NB * 8 * 2 * 4) break;
;         const int r = k >> 8, i = (r == 0) ? 1 : (r == 1) ? 3 : (r == 2) ? 2 : 0, ug = k & 255;
;         const int bh = ug >> 1, b = bh >> 3, h = bh & 7; const size_t hb = (size_t)(b * 16 + 8 + h);
;         const int base = (i >> 1) * 2 + (ug & 1), qb = (i & 1) ? 7 - base : base, w = (i & 1) ? 7 - F.wave : F.wave;
;         attn_wave<1>(QH + hb * 2048 * 64, KH + hb * 2048 * 64, VT + hb * 64 * 2048, 256 * qb + 32 * w, opaque_i(F.lane), nullptr, 0.f, nullptr, AO + (size_t)b * 2048 * DM + 512 + h * 64);
.LBB0_574:
	s_waitcnt vmcnt(0)
	s_barrier
	s_mov_b64 s[0:1], exec
	v_readlane_b32 s2, v237, 9
	v_readlane_b32 s3, v237, 10
	s_and_b64 s[2:3], s[0:1], s[2:3]
	s_mov_b64 exec, s[2:3]
	s_cbranch_execz .LBB0_578
	v_mov_b32_e32 v1, s23
	s_nop 0
	ds_write_b32 v1, v180
.LBB0_578:
	s_or_b64 exec, exec, s[0:1]
	s_waitcnt lgkmcnt(0)
	s_barrier
	ds_read_b32 v0, v138
	s_mov_b64 s[0:1], -1
	s_waitcnt lgkmcnt(0)
	v_cmp_lt_i32_e32 vcc, s24, v0
	v_readfirstlane_b32 s27, v0
	s_mov_b64 s[4:5], exec
	v_readlane_b32 s2, v237, 9
	v_readlane_b32 s3, v237, 10
	s_and_b64 s[2:3], s[4:5], s[2:3]
	s_mov_b64 exec, s[2:3]
	s_cbranch_execz .Lsbq_nxt
	v_mov_b32_e32 v180, 1
	global_atomic_add v180, v129, v180, s[18:19] sc0
.Lsbq_nxt:
	s_mov_b64 exec, s[4:5]
	s_cbranch_vccnz .LBB0_573
	s_ashr_i32 s0, s27, 8
	s_cmp_eq_u32 s0, 2
	s_cselect_b32 s1, 2, 0
	s_cmp_lg_u32 s0, 1
	s_cselect_b32 s0, s1, 3
	s_cmpk_gt_u32 s27, 0xff
	s_cselect_b32 s0, s0, 1
	s_and_b32 s1, s0, 2
	s_and_b32 s2, s27, 1
	s_or_b32 s1, s1, s2
	s_lshl_b32 s1, s1, 8
	s_bfe_u32 s28, s27, 0x30001
	s_and_b32 s0, s0, 1
	s_xor_b32 s2, s1, 0x700
	s_cmp_eq_u32 s0, 0
	s_cselect_b32 s0, s74, s22
	s_cselect_b32 s29, s1, s2
	s_lshl_b32 s0, s0, 5
	v_mov_b32_e32 v0, v208
	s_add_i32 s29, s29, s0
	v_mov_b32_e32 v47, 0
	v_and_b32_e32 v1, 31, v0
	v_or_b32_e32 v130, s29, v1
	v_ashrrev_i32_e32 v141, 5, v0
	v_ashrrev_i32_e32 v131, 31, v130
	s_cmpk_lt_i32 s29, 0xffe1
	v_mov_b32_e32 v46, v47
	v_mov_b32_e32 v45, v47
	v_mov_b32_e32 v44, v47
	v_mov_b32_e32 v43, v47
	v_mov_b32_e32 v42, v47
	v_mov_b32_e32 v41, v47
	v_mov_b32_e32 v40, v47
	v_mov_b32_e32 v39, v47
	v_mov_b32_e32 v38, v47
	v_mov_b32_e32 v37, v47
	v_mov_b32_e32 v36, v47
	v_mov_b32_e32 v35, v47
	v_mov_b32_e32 v34, v47
	v_mov_b32_e32 v33, v47
	v_mov_b32_e32 v32, v47
	v_mov_b32_e32 v63, v47
	v_mov_b32_e32 v62, v47
	v_mov_b32_e32 v61, v47
	v_mov_b32_e32 v60, v47
	v_mov_b32_e32 v59, v47
	v_mov_b32_e32 v58, v47
	v_mov_b32_e32 v57, v47
	v_mov_b32_e32 v56, v47
	v_mov_b32_e32 v55, v47
	v_mov_b32_e32 v54, v47
	v_mov_b32_e32 v53, v47
	v_mov_b32_e32 v52, v47
	v_mov_b32_e32 v51, v47
	v_mov_b32_e32 v50, v47
	v_mov_b32_e32 v49, v47
	v_mov_b32_e32 v48, v47
	s_cbranch_scc1 .LBB0_572
	s_and_b32 s0, s27, 0xf0
	s_or_b32 s0, s0, s28
	s_lshl_b32 s0, s0, 18
	s_or_b32 s4, s0, 0x200000
	v_readlane_b32 s0, v237, 58
	s_add_u32 s0, s0, s4
	v_readlane_b32 s1, v237, 59
	s_addc_u32 s1, s1, 0
	v_readlane_b32 s2, v237, 60
	s_add_u32 s2, s2, s4
	v_readlane_b32 s3, v237, 62
	s_addc_u32 s3, s3, 0
	v_lshrrev_b32_e32 v2, 1, v0
	s_ashr_i32 s6, s29, 5
	v_and_b32_e32 v9, 4, v2
	v_lshlrev_b32_e32 v2, 3, v141
	s_add_u32 s4, s96, s4
	v_lshlrev_b32_e32 v4, 1, v1
	v_ashrrev_i32_e32 v3, 31, v2
	s_addc_u32 s5, s97, 0
	v_lshlrev_b64 v[6:7], 7, v[130:131]
	v_and_b32_e32 v8, 19, v0
	v_and_b32_e32 v11, 8, v4
	v_lshlrev_b64 v[4:5], 1, v[2:3]
	v_lshl_add_u64 v[6:7], s[4:5], 0, v[6:7]
	v_or_b32_e32 v10, v9, v8
	v_lshl_add_u64 v[6:7], v[6:7], 0, v[4:5]
	global_load_dwordx4 v[64:67], v[6:7], off offset:96
	global_load_dwordx4 v[68:71], v[6:7], off offset:64
	global_load_dwordx4 v[72:75], v[6:7], off offset:32
	global_load_dwordx4 v[76:79], v[6:7], off
	v_or3_b32 v6, v10, v11, s29
	v_ashrrev_i32_e32 v7, 31, v6
	v_lshlrev_b64 v[6:7], 7, v[6:7]
	v_lshl_add_u64 v[6:7], s[0:1], 0, v[6:7]
	v_lshl_add_u64 v[6:7], v[6:7], 0, v[4:5]
	global_load_dwordx4 v[124:127], v[6:7], off
	global_load_dwordx4 v[120:123], v[6:7], off offset:32
	global_load_dwordx4 v[116:119], v[6:7], off offset:64
	global_load_dwordx4 v[112:115], v[6:7], off offset:96
	v_lshl_add_u64 v[132:133], s[2:3], 0, v[4:5]
	v_lshl_add_u64 v[134:135], s[0:1], 0, v[4:5]
	v_lshlrev_b32_e32 v4, 11, v1
	v_or_b32_e32 v6, 0x10000, v4
	v_cmp_gt_u32_e64 s[2:3], 32, v0
	v_add3_u32 v0, v8, s29, v11
	v_mov_b32_e32 v144, 0
	v_add_u32_e32 v142, s29, v2
	v_add3_u32 v143, v0, v9, s25
	s_mov_b32 s30, 0
	v_mov_b32_e32 v145, s6
	v_lshlrev_b32_e32 v128, 1, v4
	v_lshlrev_b32_e32 v136, 1, v6
	v_mov_b32_e32 v0, 0
	v_mov_b32_e32 v1, v144
	v_mov_b32_e32 v2, v144
	v_mov_b32_e32 v3, v144
	v_mov_b32_e32 v4, v144
	v_mov_b32_e32 v5, v144
	v_mov_b32_e32 v6, v144
	v_mov_b32_e32 v7, v144
	v_mov_b32_e32 v8, v144
	v_mov_b32_e32 v9, v144
	v_mov_b32_e32 v10, v144
	v_mov_b32_e32 v11, v144
	v_mov_b32_e32 v12, v144
	v_mov_b32_e32 v13, v144
	v_mov_b32_e32 v14, v144
	v_mov_b32_e32 v15, v144
	v_mov_b32_e32 v16, 0
	v_mov_b32_e32 v17, v144
	v_mov_b32_e32 v18, v144
	v_mov_b32_e32 v19, v144
	v_mov_b32_e32 v20, v144
	v_mov_b32_e32 v21, v144
	v_mov_b32_e32 v22, v144
	v_mov_b32_e32 v23, v144
	v_mov_b32_e32 v24, v144
	v_mov_b32_e32 v25, v144
	v_mov_b32_e32 v26, v144
	v_mov_b32_e32 v27, v144
	v_mov_b32_e32 v28, v144
	v_mov_b32_e32 v29, v144
	v_mov_b32_e32 v30, v144
	v_mov_b32_e32 v31, v144
